# v26 + LayerNorm-1 row loop: next row requested one row ahead, gain/bias pieces read once per phase, row-top wait counts only the row's own five stores
# speedup vs baseline: 1.0171x; 1.0067x over previous
.LBB0_1198:
	s_and_saveexec_b64 s[0:1], s[2:3]
	ds_write_b32 v47, v3
	s_or_b64 exec, exec, s[0:1]
	s_ashr_i32 s29, s28, 31
	s_lshl_b64 s[0:1], s[28:29], 2
	s_add_u32 s12, s0, 0x3d600000
	s_addc_u32 s13, s1, 0
	s_lshl_b64 s[0:1], s[28:29], 11
	s_ashr_i32 s31, s30, 31
	v_mov_b32_e32 v55, s1
	v_or_b32_e32 v54, s0, v46
	s_lshl_b64 s[0:1], s[30:31], 2
	s_add_u32 s14, s0, 0x3d600000
	s_addc_u32 s15, s1, 0
	s_lshl_b64 s[0:1], s[30:31], 11
	s_ashr_i32 s35, s34, 31
	v_mov_b32_e32 v57, s1
	v_or_b32_e32 v56, s0, v46
	s_lshl_b64 s[0:1], s[34:35], 2
	s_add_u32 s16, s0, 0x3d600000
	s_addc_u32 s17, s1, 0
	s_lshl_b64 s[0:1], s[34:35], 11
	v_mov_b32_e32 v59, s1
	v_or_b32_e32 v58, s0, v46
	s_bfe_i64 s[0:1], s[36:37], 0x200000
	s_lshl_b64 s[8:9], s[0:1], 2
	s_add_u32 s38, s8, 0x3d600000
	s_addc_u32 s39, s9, 0
	s_lshl_b64 s[8:9], s[0:1], 11
	v_mov_b32_e32 v61, s9
	v_or_b32_e32 v60, s8, v46
	s_mov_b64 s[8:9], 0
	global_load_dwordx4 v[160:163], v[42:43], off offset:2048
	global_load_dwordx4 v[164:167], v[44:45], off offset:2048
	global_load_dwordx4 v[168:171], v[42:43], off offset:2064
	global_load_dwordx4 v[172:175], v[44:45], off offset:2064
	global_load_dwordx4 v[176:179], v[42:43], off offset:16
	global_load_dwordx4 v[180:183], v[42:43], off
	global_load_dwordx4 v[184:187], v[44:45], off offset:16
	global_load_dwordx4 v[188:191], v[44:45], off
	v_lshl_add_u64 v[124:125], s[18:19], 0, v[60:61]
	v_add_co_u32_e32 v124, vcc, 0x2f200000, v124
	s_nop 1
	v_addc_co_u32_e32 v125, vcc, 0, v125, vcc
	global_load_dwordx4 v[128:131], v[124:125], off
	global_load_dwordx4 v[124:127], v[124:125], off offset:1024
	s_waitcnt vmcnt(0)
	s_branch .LBB0_1202

.LBB0_1202:
	v_lshl_add_u64 v[78:79], s[18:19], 0, v[60:61]
	s_mov_b32 s10, 0x2f200000
	v_add_co_u32_e32 v4, vcc, s10, v78
	s_mov_b32 s11, 0x2e00000
	s_nop 0
	v_addc_co_u32_e32 v5, vcc, 0, v79, vcc
	s_waitcnt vmcnt(5)
	v_mov_b64_e32 v[8:9], v[124:125]
	v_mov_b64_e32 v[10:11], v[126:127]
	v_mov_b64_e32 v[12:13], v[128:129]
	v_mov_b64_e32 v[14:15], v[130:131]
	v_lshl_add_u64 v[124:125], s[18:19], 0, v[58:59]
	v_add_co_u32_e32 v124, vcc, 0x2f200000, v124
	s_nop 1
	v_addc_co_u32_e32 v125, vcc, 0, v125, vcc
	global_load_dwordx4 v[128:131], v[124:125], off
	global_load_dwordx4 v[124:127], v[124:125], off offset:1024
	s_nop 0
	v_mov_b64_e32 v[4:5], v[160:161]
	v_mov_b64_e32 v[6:7], v[162:163]
	v_add_co_u32_e32 v78, vcc, s11, v78
	s_add_u32 s40, s36, s8
	s_nop 0
	v_addc_co_u32_e32 v79, vcc, 0, v79, vcc
	s_add_u32 s10, s0, s8
	s_addc_u32 s11, s1, s9
	s_add_i32 s41, s40, 0xffffc000
	s_cmpk_lt_i32 s40, 0x4000
	s_cselect_b32 s10, s10, s41
	s_mov_b32 s41, 0x3e200000
	s_cselect_b32 s41, s41, 0x45200000
	s_cselect_b32 s11, s11, 0
	s_add_u32 s41, s18, s41
	s_addc_u32 s42, s19, 0
	s_lshl_b64 s[10:11], s[10:11], 10
	s_add_u32 s10, s41, s10
	s_addc_u32 s11, s42, s11
	v_lshlrev_b32_e32 v62, 16, v8
	v_lshlrev_b32_e32 v70, 16, v12
	v_and_b32_e32 v72, 0xffff0000, v12
	v_add_f32_e32 v2, 0, v70
	v_lshlrev_b32_e32 v71, 16, v13
	v_add_f32_e32 v2, v2, v72
	v_and_b32_e32 v73, 0xffff0000, v13
	v_add_f32_e32 v2, v2, v71
	v_lshlrev_b32_e32 v74, 16, v14
	v_add_f32_e32 v2, v2, v73
	v_and_b32_e32 v76, 0xffff0000, v14
	v_add_f32_e32 v2, v2, v74
	v_lshlrev_b32_e32 v75, 16, v15
	v_add_f32_e32 v2, v2, v76
	v_and_b32_e32 v77, 0xffff0000, v15
	v_add_f32_e32 v2, v2, v75
	v_add_f32_e32 v2, v2, v77
	v_and_b32_e32 v64, 0xffff0000, v8
	v_add_f32_e32 v2, v2, v62
	v_lshlrev_b32_e32 v63, 16, v9
	v_add_f32_e32 v2, v2, v64
	v_and_b32_e32 v65, 0xffff0000, v9
	v_add_f32_e32 v2, v2, v63
	v_lshlrev_b32_e32 v66, 16, v10
	v_add_f32_e32 v2, v2, v65
	v_and_b32_e32 v68, 0xffff0000, v10
	v_add_f32_e32 v2, v2, v66
	v_lshlrev_b32_e32 v67, 16, v11
	v_add_f32_e32 v2, v2, v68
	v_and_b32_e32 v69, 0xffff0000, v11
	v_add_f32_e32 v2, v2, v67
	v_add_f32_e32 v2, v2, v69
	ds_bpermute_b32 v12, v80, v2
	v_mov_b64_e32 v[8:9], v[164:165]
	v_mov_b64_e32 v[10:11], v[166:167]
	s_waitcnt lgkmcnt(0)
	v_add_f32_e32 v2, v2, v12
	v_mov_b64_e32 v[12:13], v[168:169]
	v_mov_b64_e32 v[14:15], v[170:171]
	v_mov_b64_e32 v[16:17], v[172:173]
	v_mov_b64_e32 v[18:19], v[174:175]
	ds_bpermute_b32 v20, v81, v2
	s_waitcnt lgkmcnt(0)
	v_add_f32_e32 v2, v2, v20
	v_mov_b64_e32 v[20:21], v[176:177]
	v_mov_b64_e32 v[22:23], v[178:179]
	v_mov_b64_e32 v[24:25], v[180:181]
	v_mov_b64_e32 v[26:27], v[182:183]
	v_mov_b64_e32 v[28:29], v[184:185]
	v_mov_b64_e32 v[30:31], v[186:187]
	v_mov_b64_e32 v[32:33], v[188:189]
	v_mov_b64_e32 v[34:35], v[190:191]
	ds_bpermute_b32 v53, v82, v2
	s_waitcnt lgkmcnt(0)
	v_add_f32_e32 v2, v2, v53
	ds_bpermute_b32 v53, v83, v2
	s_waitcnt lgkmcnt(0)
	v_add_f32_e32 v2, v2, v53
	ds_bpermute_b32 v53, v84, v2
	s_waitcnt lgkmcnt(0)
	v_add_f32_e32 v2, v2, v53
	ds_bpermute_b32 v53, v85, v2
	s_waitcnt lgkmcnt(0)
	v_add_f32_e32 v2, v2, v53
	v_mul_f32_e32 v2, 0x3a800000, v2
	v_pk_add_f32 v[70:71], v[70:71], v[2:3] op_sel_hi:[1,0] neg_lo:[0,1] neg_hi:[0,1]
	v_pk_add_f32 v[72:73], v[72:73], v[2:3] op_sel_hi:[1,0] neg_lo:[0,1] neg_hi:[0,1]
	v_pk_mul_f32 v[108:109], v[70:71], v[70:71]
	v_pk_mul_f32 v[110:111], v[72:73], v[72:73]
	v_pk_add_f32 v[74:75], v[74:75], v[2:3] op_sel_hi:[1,0] neg_lo:[0,1] neg_hi:[0,1]
	v_pk_add_f32 v[76:77], v[76:77], v[2:3] op_sel_hi:[1,0] neg_lo:[0,1] neg_hi:[0,1]
	v_pk_add_f32 v[62:63], v[62:63], v[2:3] op_sel_hi:[1,0] neg_lo:[0,1] neg_hi:[0,1]
	v_pk_add_f32 v[64:65], v[64:65], v[2:3] op_sel_hi:[1,0] neg_lo:[0,1] neg_hi:[0,1]
	v_pk_add_f32 v[66:67], v[66:67], v[2:3] op_sel_hi:[1,0] neg_lo:[0,1] neg_hi:[0,1]
	v_pk_add_f32 v[68:69], v[68:69], v[2:3] op_sel_hi:[1,0] neg_lo:[0,1] neg_hi:[0,1]
	v_add_f32_e32 v2, v108, v110
	v_add_f32_e32 v2, v109, v2
	v_pk_mul_f32 v[112:113], v[74:75], v[74:75]
	v_add_f32_e32 v2, v111, v2
	v_pk_mul_f32 v[114:115], v[76:77], v[76:77]
	v_add_f32_e32 v2, v112, v2
	v_add_f32_e32 v2, v114, v2
	v_add_f32_e32 v2, v113, v2
	v_pk_mul_f32 v[116:117], v[62:63], v[62:63]
	v_add_f32_e32 v2, v115, v2
	v_pk_mul_f32 v[118:119], v[64:65], v[64:65]
	v_add_f32_e32 v2, v116, v2
	v_add_f32_e32 v2, v118, v2
	v_mov_b32_e32 v120, v68
	v_mov_b32_e32 v121, v66
	v_add_f32_e32 v2, v117, v2
	v_pk_mul_f32 v[120:121], v[120:121], v[120:121]
	v_add_f32_e32 v2, v119, v2
	v_mov_b32_e32 v122, v69
	v_mov_b32_e32 v123, v67
	v_add_f32_e32 v2, v121, v2
	v_pk_mul_f32 v[122:123], v[122:123], v[122:123]
	v_add_f32_e32 v2, v120, v2
	v_add_f32_e32 v2, v123, v2
	v_add_f32_e32 v2, v122, v2
	ds_bpermute_b32 v53, v80, v2
	v_mov_b32_e32 v108, v4
	v_mov_b32_e32 v109, v6
	v_mov_b32_e32 v6, v5
	s_waitcnt lgkmcnt(0)
	v_add_f32_e32 v2, v2, v53
	ds_bpermute_b32 v4, v81, v2
	v_mov_b32_e32 v110, v8
	v_mov_b32_e32 v111, v10
	v_mov_b32_e32 v10, v9
	s_waitcnt lgkmcnt(0)
	v_add_f32_e32 v2, v2, v4
	ds_bpermute_b32 v53, v82, v2
	v_mov_b32_e32 v8, v16
	v_mov_b32_e32 v4, v12
	v_mov_b32_e32 v5, v14
	v_mov_b32_e32 v9, v18
	s_waitcnt lgkmcnt(0)
	v_add_f32_e32 v2, v2, v53
	ds_bpermute_b32 v16, v83, v2
	v_mov_b32_e32 v12, v24
	v_mov_b32_e32 v14, v13
	v_mov_b32_e32 v18, v17
	v_mov_b32_e32 v13, v26
	s_waitcnt lgkmcnt(0)
	v_add_f32_e32 v2, v2, v16
	ds_bpermute_b32 v24, v84, v2
	v_mov_b32_e32 v16, v32
	v_mov_b32_e32 v17, v34
	v_mov_b32_e32 v26, v25
	v_mov_b32_e32 v34, v33
	s_waitcnt lgkmcnt(0)
	v_add_f32_e32 v2, v2, v24
	ds_bpermute_b32 v53, v85, v2
	v_mov_b32_e32 v24, v20
	v_mov_b32_e32 v25, v22
	v_mov_b32_e32 v32, v28
	v_mov_b32_e32 v33, v30
	s_waitcnt lgkmcnt(0)
	v_add_f32_e32 v2, v2, v53
	v_fmamk_f32 v2, v2, 0x3a800000, v237
	v_mul_f32_e32 v20, 0x4b800000, v2
	v_cmp_gt_f32_e32 vcc, s85, v2
	v_mov_b32_e32 v22, v21
	v_mov_b32_e32 v30, v29
	v_cndmask_b32_e32 v2, v2, v20, vcc
	v_rsq_f32_e32 v2, v2
	s_nop 0
	v_mul_f32_e32 v20, 0x45800000, v2
	v_cndmask_b32_e32 v2, v2, v20, vcc
	v_pk_mul_f32 v[20:21], v[70:71], v[2:3] op_sel_hi:[1,0]
	v_pk_mul_f32 v[28:29], v[74:75], v[2:3] op_sel_hi:[1,0]
	v_pk_mul_f32 v[70:71], v[72:73], v[2:3] op_sel_hi:[1,0]
	v_pk_mul_f32 v[64:65], v[64:65], v[2:3] op_sel_hi:[1,0]
	v_pk_fma_f32 v[12:13], v[12:13], v[20:21], v[16:17]
	v_pk_fma_f32 v[16:17], v[24:25], v[28:29], v[32:33]
	v_pk_fma_f32 v[20:21], v[26:27], v[70:71], v[34:35]
	v_pk_mul_f32 v[72:73], v[76:77], v[2:3] op_sel_hi:[1,0]
	v_pk_fma_f32 v[28:29], v[6:7], v[64:65], v[10:11]
	v_bfe_u32 v6, v20, 16, 1
	v_bfe_u32 v10, v17, 16, 1
	v_max3_f32 v35, |v12|, 0, |v20|
	v_pk_fma_f32 v[22:23], v[22:23], v[72:73], v[30:31]
	v_add3_u32 v53, v20, v6, s86
	v_add3_u32 v6, v17, v10, s86
	v_max3_f32 v10, v35, |v13|, |v21|
	v_pk_mul_f32 v[62:63], v[62:63], v[2:3] op_sel_hi:[1,0]
	v_max3_f32 v10, v10, |v16|, |v22|
	v_pk_fma_f32 v[24:25], v[108:109], v[62:63], v[110:111]
	v_max3_f32 v10, v10, |v17|, |v23|
	v_pk_mul_f32 v[66:67], v[66:67], v[2:3] op_sel_hi:[1,0]
	v_pk_mul_f32 v[68:69], v[68:69], v[2:3] op_sel_hi:[1,0]
	v_max3_f32 v10, v10, |v24|, |v28|
	v_pk_fma_f32 v[26:27], v[4:5], v[66:67], v[8:9]
	v_pk_fma_f32 v[14:15], v[14:15], v[68:69], v[18:19]
	v_max3_f32 v10, v10, |v25|, |v29|
	v_max3_f32 v10, v10, |v26|, |v14|
	v_max3_f32 v10, v10, |v27|, |v15|
	ds_bpermute_b32 v35, v80, v10
	v_bfe_u32 v7, v12, 16, 1
	v_add3_u32 v7, v12, v7, s86
	v_lshrrev_b32_e32 v62, 16, v7
	v_bfe_u32 v2, v23, 16, 1
	s_waitcnt lgkmcnt(0)
	v_max_f32_e32 v35, v35, v35
	v_max_f32_e32 v10, v10, v35
	ds_bpermute_b32 v35, v81, v10
	v_add3_u32 v2, v23, v2, s86
	v_lshrrev_b32_e32 v6, 16, v6
	v_bfe_u32 v8, v13, 16, 1
	v_bfe_u32 v5, v21, 16, 1
	s_waitcnt lgkmcnt(0)
	v_max_f32_e32 v7, v35, v35
	v_max_f32_e32 v7, v10, v7
	ds_bpermute_b32 v10, v82, v7
	v_add3_u32 v8, v13, v8, s86
	v_bfe_u32 v34, v27, 16, 1
	v_add3_u32 v5, v21, v5, s86
	v_lshrrev_b32_e32 v8, 16, v8
	s_waitcnt lgkmcnt(0)
	v_max_f32_e32 v10, v10, v10
	v_max_f32_e32 v10, v7, v10
	ds_bpermute_b32 v35, v83, v10
	v_and_or_b32 v7, v2, s87, v6
	v_bfe_u32 v11, v15, 16, 1
	v_add3_u32 v34, v27, v34, s86
	v_and_or_b32 v5, v5, s87, v8
	s_waitcnt lgkmcnt(0)
	v_max_f32_e32 v2, v35, v35
	v_max_f32_e32 v2, v10, v2
	ds_bpermute_b32 v10, v84, v2
	v_add3_u32 v11, v15, v11, s86
	v_lshrrev_b32_e32 v34, 16, v34
	v_and_or_b32 v11, v11, s87, v34
	v_bfe_u32 v9, v16, 16, 1
	s_waitcnt lgkmcnt(0)
	v_max_f32_e32 v8, v10, v10
	v_max_f32_e32 v2, v2, v8
	ds_bpermute_b32 v34, v85, v2
	v_bfe_u32 v4, v22, 16, 1
	v_add3_u32 v9, v16, v9, s86
	v_add3_u32 v4, v22, v4, s86
	v_lshrrev_b32_e32 v9, 16, v9
	v_and_or_b32 v6, v4, s87, v9
	v_and_or_b32 v4, v53, s87, v62
	s_waitcnt lgkmcnt(0)
	v_max3_f32 v2, v2, v34, s55
	global_store_dwordx4 v[78:79], v[4:7], off
	v_bfe_u32 v31, v24, 16, 1
	v_bfe_u32 v32, v25, 16, 1
	v_div_scale_f32 v4, s[42:43], v2, v2, s80
	v_rcp_f32_e32 v5, v4
	v_bfe_u32 v33, v26, 16, 1
	v_bfe_u32 v18, v14, 16, 1
	v_bfe_u32 v19, v29, 16, 1
	v_bfe_u32 v30, v28, 16, 1
	v_add3_u32 v33, v26, v33, s86
	v_add3_u32 v32, v25, v32, s86
	v_add3_u32 v31, v24, v31, s86
	v_fma_f32 v7, -v4, v5, 1.0
	v_add3_u32 v30, v28, v30, s86
	v_add3_u32 v19, v29, v19, s86
	v_add3_u32 v18, v14, v18, s86
	v_lshrrev_b32_e32 v31, 16, v31
	v_lshrrev_b32_e32 v32, 16, v32
	v_lshrrev_b32_e32 v33, 16, v33
	v_div_scale_f32 v6, vcc, s80, v2, s80
	v_fmac_f32_e32 v5, v7, v5
	v_and_or_b32 v10, v18, s87, v33
	v_and_or_b32 v9, v19, s87, v32
	v_and_or_b32 v8, v30, s87, v31
	v_mul_f32_e32 v7, v6, v5
	global_store_dwordx4 v[78:79], v[8:11], off offset:1024
	s_nop 1
	v_fma_f32 v8, -v4, v7, v6
	v_fmac_f32_e32 v7, v8, v5
	v_fma_f32 v4, -v4, v7, v6
	v_div_fmas_f32 v4, v4, v5, v7
	v_div_fixup_f32 v4, v4, v2, s80
	v_mul_f32_e32 v5, v12, v4
	v_mul_f32_e32 v6, v20, v4
	v_rndne_f32_e32 v5, v5
	v_mul_f32_e32 v7, v13, v4
	v_mul_f32_e32 v8, v21, v4
	v_mul_f32_e32 v9, v16, v4
	v_mul_f32_e32 v10, v22, v4
	v_mul_f32_e32 v11, v17, v4
	v_mul_f32_e32 v12, v23, v4
	v_mul_f32_e32 v13, v24, v4
	v_mul_f32_e32 v16, v28, v4
	v_mul_f32_e32 v17, v25, v4
	v_mul_f32_e32 v18, v29, v4
	v_mul_f32_e32 v19, v26, v4
	v_mul_f32_e32 v14, v14, v4
	v_mul_f32_e32 v20, v27, v4
	v_mul_f32_e32 v4, v15, v4
	v_rndne_f32_e32 v6, v6
	v_rndne_f32_e32 v15, v4
	v_add_f32_e32 v4, 0x43000000, v5
	v_rndne_f32_e32 v7, v7
	v_cvt_pk_u8_f32 v4, v4, 0, 0
	v_add_f32_e32 v5, 0x43000000, v6
	v_rndne_f32_e32 v8, v8
	v_cvt_pk_u8_f32 v4, v5, 1, v4
	v_add_f32_e32 v5, 0x43000000, v7
	v_rndne_f32_e32 v9, v9
	v_cvt_pk_u8_f32 v4, v5, 2, v4
	v_add_f32_e32 v5, 0x43000000, v8
	v_rndne_f32_e32 v10, v10
	v_cvt_pk_u8_f32 v4, v5, 3, v4
	v_add_f32_e32 v5, 0x43000000, v9
	v_rndne_f32_e32 v11, v11
	v_cvt_pk_u8_f32 v5, v5, 0, 0
	v_add_f32_e32 v6, 0x43000000, v10
	v_rndne_f32_e32 v12, v12
	v_cvt_pk_u8_f32 v5, v6, 1, v5
	v_add_f32_e32 v6, 0x43000000, v11
	v_rndne_f32_e32 v13, v13
	v_cvt_pk_u8_f32 v5, v6, 2, v5
	v_add_f32_e32 v6, 0x43000000, v12
	v_rndne_f32_e32 v16, v16
	v_cvt_pk_u8_f32 v5, v6, 3, v5
	v_add_f32_e32 v6, 0x43000000, v13
	v_rndne_f32_e32 v17, v17
	v_cvt_pk_u8_f32 v6, v6, 0, 0
	v_add_f32_e32 v7, 0x43000000, v16
	v_rndne_f32_e32 v18, v18
	v_cvt_pk_u8_f32 v6, v7, 1, v6
	v_add_f32_e32 v7, 0x43000000, v17
	v_rndne_f32_e32 v19, v19
	v_cvt_pk_u8_f32 v6, v7, 2, v6
	v_add_f32_e32 v7, 0x43000000, v18
	v_rndne_f32_e32 v14, v14
	v_cvt_pk_u8_f32 v6, v7, 3, v6
	v_add_f32_e32 v7, 0x43000000, v19
	v_rndne_f32_e32 v20, v20
	v_cvt_pk_u8_f32 v7, v7, 0, 0
	v_add_f32_e32 v8, 0x43000000, v14
	v_cvt_pk_u8_f32 v7, v8, 1, v7
	v_add_f32_e32 v8, 0x43000000, v20
	v_cvt_pk_u8_f32 v7, v8, 2, v7
	v_add_f32_e32 v8, 0x43000000, v15
	v_xor_b32_e32 v4, 0x80808080, v4
	v_xor_b32_e32 v5, 0x80808080, v5
	v_cvt_pk_u8_f32 v7, v8, 3, v7
	v_lshl_add_u64 v[8:9], s[10:11], 0, v[38:39]
	v_xor_b32_e32 v6, 0x80808080, v6
	v_xor_b32_e32 v7, 0x80808080, v7
	global_store_dwordx2 v[8:9], v[4:5], off
	global_store_dwordx2 v[8:9], v[6:7], off offset:512
	s_and_saveexec_b64 s[10:11], s[4:5]
	s_cbranch_execz .LBB0_1204
	s_add_u32 s42, s18, s38
	s_addc_u32 s43, s19, s39
	v_mul_f32_e32 v2, 0x3c010204, v2
	global_store_dword v3, v2, s[42:43]
.LBB0_1204:
	s_or_b64 exec, exec, s[10:11]
	v_lshl_add_u64 v[78:79], s[18:19], 0, v[58:59]
	v_add_co_u32_e32 v4, vcc, 0x2f200000, v78
	s_mov_b32 s41, 0x2e00000
	s_nop 0
	v_addc_co_u32_e32 v5, vcc, 0, v79, vcc
	s_waitcnt vmcnt(5)
	v_mov_b64_e32 v[8:9], v[124:125]
	v_mov_b64_e32 v[10:11], v[126:127]
	v_mov_b64_e32 v[12:13], v[128:129]
	v_mov_b64_e32 v[14:15], v[130:131]
	v_lshl_add_u64 v[124:125], s[18:19], 0, v[56:57]
	v_add_co_u32_e32 v124, vcc, 0x2f200000, v124
	s_nop 1
	v_addc_co_u32_e32 v125, vcc, 0, v125, vcc
	global_load_dwordx4 v[128:131], v[124:125], off
	global_load_dwordx4 v[124:127], v[124:125], off offset:1024
	s_nop 0
	v_mov_b64_e32 v[4:5], v[160:161]
	v_mov_b64_e32 v[6:7], v[162:163]
	v_add_co_u32_e32 v78, vcc, s41, v78
	s_add_i32 s10, s40, 1
	s_nop 0
	v_addc_co_u32_e32 v79, vcc, 0, v79, vcc
	s_add_u32 s11, s34, s8
	s_addc_u32 s41, s35, s9
	s_add_i32 s42, s40, 0xffffc001
	s_cmpk_lt_i32 s10, 0x4000
	s_mov_b32 s10, 0x3e200000
	s_cselect_b32 s10, s10, 0x45200000
	s_cselect_b32 s43, s41, 0
	s_cselect_b32 s42, s11, s42
	s_add_u32 s41, s18, s10
	s_addc_u32 s44, s19, 0
	s_lshl_b64 s[10:11], s[42:43], 10
	s_add_u32 s10, s41, s10
	s_addc_u32 s11, s44, s11
	v_lshlrev_b32_e32 v62, 16, v8
	v_lshlrev_b32_e32 v70, 16, v12
	v_and_b32_e32 v72, 0xffff0000, v12
	v_add_f32_e32 v2, 0, v70
	v_lshlrev_b32_e32 v71, 16, v13
	v_add_f32_e32 v2, v2, v72
	v_and_b32_e32 v73, 0xffff0000, v13
	v_add_f32_e32 v2, v2, v71
	v_lshlrev_b32_e32 v74, 16, v14
	v_add_f32_e32 v2, v2, v73
	v_and_b32_e32 v76, 0xffff0000, v14
	v_add_f32_e32 v2, v2, v74
	v_lshlrev_b32_e32 v75, 16, v15
	v_add_f32_e32 v2, v2, v76
	v_and_b32_e32 v77, 0xffff0000, v15
	v_add_f32_e32 v2, v2, v75
	v_add_f32_e32 v2, v2, v77
	v_and_b32_e32 v64, 0xffff0000, v8
	v_add_f32_e32 v2, v2, v62
	v_lshlrev_b32_e32 v63, 16, v9
	v_add_f32_e32 v2, v2, v64
	v_and_b32_e32 v65, 0xffff0000, v9
	v_add_f32_e32 v2, v2, v63
	v_lshlrev_b32_e32 v66, 16, v10
	v_add_f32_e32 v2, v2, v65
	v_and_b32_e32 v68, 0xffff0000, v10
	v_add_f32_e32 v2, v2, v66
	v_lshlrev_b32_e32 v67, 16, v11
	v_add_f32_e32 v2, v2, v68
	v_and_b32_e32 v69, 0xffff0000, v11
	v_add_f32_e32 v2, v2, v67
	v_add_f32_e32 v2, v2, v69
	ds_bpermute_b32 v12, v80, v2
	v_mov_b64_e32 v[8:9], v[164:165]
	v_mov_b64_e32 v[10:11], v[166:167]
	s_waitcnt lgkmcnt(0)
	v_add_f32_e32 v2, v2, v12
	v_mov_b64_e32 v[12:13], v[168:169]
	v_mov_b64_e32 v[14:15], v[170:171]
	v_mov_b64_e32 v[16:17], v[172:173]
	v_mov_b64_e32 v[18:19], v[174:175]
	ds_bpermute_b32 v20, v81, v2
	s_waitcnt lgkmcnt(0)
	v_add_f32_e32 v2, v2, v20
	v_mov_b64_e32 v[20:21], v[176:177]
	v_mov_b64_e32 v[22:23], v[178:179]
	v_mov_b64_e32 v[24:25], v[180:181]
	v_mov_b64_e32 v[26:27], v[182:183]
	v_mov_b64_e32 v[28:29], v[184:185]
	v_mov_b64_e32 v[30:31], v[186:187]
	v_mov_b64_e32 v[32:33], v[188:189]
	v_mov_b64_e32 v[34:35], v[190:191]
	ds_bpermute_b32 v53, v82, v2
	s_waitcnt lgkmcnt(0)
	v_add_f32_e32 v2, v2, v53
	ds_bpermute_b32 v53, v83, v2
	s_waitcnt lgkmcnt(0)
	v_add_f32_e32 v2, v2, v53
	ds_bpermute_b32 v53, v84, v2
	s_waitcnt lgkmcnt(0)
	v_add_f32_e32 v2, v2, v53
	ds_bpermute_b32 v53, v85, v2
	s_waitcnt lgkmcnt(0)
	v_add_f32_e32 v2, v2, v53
	v_mul_f32_e32 v2, 0x3a800000, v2
	v_pk_add_f32 v[70:71], v[70:71], v[2:3] op_sel_hi:[1,0] neg_lo:[0,1] neg_hi:[0,1]
	v_pk_add_f32 v[72:73], v[72:73], v[2:3] op_sel_hi:[1,0] neg_lo:[0,1] neg_hi:[0,1]
	v_pk_mul_f32 v[108:109], v[70:71], v[70:71]
	v_pk_mul_f32 v[110:111], v[72:73], v[72:73]
	v_pk_add_f32 v[74:75], v[74:75], v[2:3] op_sel_hi:[1,0] neg_lo:[0,1] neg_hi:[0,1]
	v_pk_add_f32 v[76:77], v[76:77], v[2:3] op_sel_hi:[1,0] neg_lo:[0,1] neg_hi:[0,1]
	v_pk_add_f32 v[62:63], v[62:63], v[2:3] op_sel_hi:[1,0] neg_lo:[0,1] neg_hi:[0,1]
	v_pk_add_f32 v[64:65], v[64:65], v[2:3] op_sel_hi:[1,0] neg_lo:[0,1] neg_hi:[0,1]
	v_pk_add_f32 v[66:67], v[66:67], v[2:3] op_sel_hi:[1,0] neg_lo:[0,1] neg_hi:[0,1]
	v_pk_add_f32 v[68:69], v[68:69], v[2:3] op_sel_hi:[1,0] neg_lo:[0,1] neg_hi:[0,1]
	v_add_f32_e32 v2, v108, v110
	v_add_f32_e32 v2, v109, v2
	v_pk_mul_f32 v[112:113], v[74:75], v[74:75]
	v_add_f32_e32 v2, v111, v2
	v_pk_mul_f32 v[114:115], v[76:77], v[76:77]
	v_add_f32_e32 v2, v112, v2
	v_add_f32_e32 v2, v114, v2
	v_add_f32_e32 v2, v113, v2
	v_pk_mul_f32 v[116:117], v[62:63], v[62:63]
	v_add_f32_e32 v2, v115, v2
	v_pk_mul_f32 v[118:119], v[64:65], v[64:65]
	v_add_f32_e32 v2, v116, v2
	v_add_f32_e32 v2, v118, v2
	v_mov_b32_e32 v120, v68
	v_mov_b32_e32 v121, v66
	v_add_f32_e32 v2, v117, v2
	v_pk_mul_f32 v[120:121], v[120:121], v[120:121]
	v_add_f32_e32 v2, v119, v2
	v_mov_b32_e32 v122, v69
	v_mov_b32_e32 v123, v67
	v_add_f32_e32 v2, v121, v2
	v_pk_mul_f32 v[122:123], v[122:123], v[122:123]
	v_add_f32_e32 v2, v120, v2
	v_add_f32_e32 v2, v123, v2
	v_add_f32_e32 v2, v122, v2
	ds_bpermute_b32 v53, v80, v2
	v_mov_b32_e32 v108, v4
	v_mov_b32_e32 v109, v6
	v_mov_b32_e32 v6, v5
	s_waitcnt lgkmcnt(0)
	v_add_f32_e32 v2, v2, v53
	ds_bpermute_b32 v4, v81, v2
	v_mov_b32_e32 v110, v8
	v_mov_b32_e32 v111, v10
	v_mov_b32_e32 v10, v9
	s_waitcnt lgkmcnt(0)
	v_add_f32_e32 v2, v2, v4
	ds_bpermute_b32 v53, v82, v2
	v_mov_b32_e32 v8, v16
	v_mov_b32_e32 v4, v12
	v_mov_b32_e32 v5, v14
	v_mov_b32_e32 v9, v18
	s_waitcnt lgkmcnt(0)
	v_add_f32_e32 v2, v2, v53
	ds_bpermute_b32 v16, v83, v2
	v_mov_b32_e32 v12, v24
	v_mov_b32_e32 v14, v13
	v_mov_b32_e32 v18, v17
	v_mov_b32_e32 v13, v26
	s_waitcnt lgkmcnt(0)
	v_add_f32_e32 v2, v2, v16
	ds_bpermute_b32 v24, v84, v2
	v_mov_b32_e32 v16, v32
	v_mov_b32_e32 v17, v34
	v_mov_b32_e32 v26, v25
	v_mov_b32_e32 v34, v33
	s_waitcnt lgkmcnt(0)
	v_add_f32_e32 v2, v2, v24
	ds_bpermute_b32 v53, v85, v2
	v_mov_b32_e32 v24, v20
	v_mov_b32_e32 v25, v22
	v_mov_b32_e32 v32, v28
	v_mov_b32_e32 v33, v30
	s_waitcnt lgkmcnt(0)
	v_add_f32_e32 v2, v2, v53
	v_fmamk_f32 v2, v2, 0x3a800000, v237
	v_mul_f32_e32 v20, 0x4b800000, v2
	v_cmp_gt_f32_e32 vcc, s85, v2
	v_mov_b32_e32 v22, v21
	v_mov_b32_e32 v30, v29
	v_cndmask_b32_e32 v2, v2, v20, vcc
	v_rsq_f32_e32 v2, v2
	s_nop 0
	v_mul_f32_e32 v20, 0x45800000, v2
	v_cndmask_b32_e32 v2, v2, v20, vcc
	v_pk_mul_f32 v[20:21], v[70:71], v[2:3] op_sel_hi:[1,0]
	v_pk_mul_f32 v[28:29], v[74:75], v[2:3] op_sel_hi:[1,0]
	v_pk_mul_f32 v[70:71], v[72:73], v[2:3] op_sel_hi:[1,0]
	v_pk_mul_f32 v[64:65], v[64:65], v[2:3] op_sel_hi:[1,0]
	v_pk_fma_f32 v[12:13], v[12:13], v[20:21], v[16:17]
	v_pk_fma_f32 v[16:17], v[24:25], v[28:29], v[32:33]
	v_pk_fma_f32 v[20:21], v[26:27], v[70:71], v[34:35]
	v_pk_mul_f32 v[72:73], v[76:77], v[2:3] op_sel_hi:[1,0]
	v_pk_fma_f32 v[28:29], v[6:7], v[64:65], v[10:11]
	v_bfe_u32 v6, v20, 16, 1
	v_bfe_u32 v10, v17, 16, 1
	v_max3_f32 v35, |v12|, 0, |v20|
	v_pk_fma_f32 v[22:23], v[22:23], v[72:73], v[30:31]
	v_add3_u32 v53, v20, v6, s86
	v_add3_u32 v6, v17, v10, s86
	v_max3_f32 v10, v35, |v13|, |v21|
	v_pk_mul_f32 v[62:63], v[62:63], v[2:3] op_sel_hi:[1,0]
	v_max3_f32 v10, v10, |v16|, |v22|
	v_pk_fma_f32 v[24:25], v[108:109], v[62:63], v[110:111]
	v_max3_f32 v10, v10, |v17|, |v23|
	v_pk_mul_f32 v[66:67], v[66:67], v[2:3] op_sel_hi:[1,0]
	v_pk_mul_f32 v[68:69], v[68:69], v[2:3] op_sel_hi:[1,0]
	v_max3_f32 v10, v10, |v24|, |v28|
	v_pk_fma_f32 v[26:27], v[4:5], v[66:67], v[8:9]
	v_pk_fma_f32 v[14:15], v[14:15], v[68:69], v[18:19]
	v_max3_f32 v10, v10, |v25|, |v29|
	v_max3_f32 v10, v10, |v26|, |v14|
	v_max3_f32 v10, v10, |v27|, |v15|
	ds_bpermute_b32 v35, v80, v10
	v_bfe_u32 v7, v12, 16, 1
	v_add3_u32 v7, v12, v7, s86
	v_lshrrev_b32_e32 v62, 16, v7
	v_bfe_u32 v2, v23, 16, 1
	s_waitcnt lgkmcnt(0)
	v_max_f32_e32 v35, v35, v35
	v_max_f32_e32 v10, v10, v35
	ds_bpermute_b32 v35, v81, v10
	v_add3_u32 v2, v23, v2, s86
	v_lshrrev_b32_e32 v6, 16, v6
	v_bfe_u32 v8, v13, 16, 1
	v_bfe_u32 v5, v21, 16, 1
	s_waitcnt lgkmcnt(0)
	v_max_f32_e32 v7, v35, v35
	v_max_f32_e32 v7, v10, v7
	ds_bpermute_b32 v10, v82, v7
	v_add3_u32 v8, v13, v8, s86
	v_bfe_u32 v34, v27, 16, 1
	v_add3_u32 v5, v21, v5, s86
	v_lshrrev_b32_e32 v8, 16, v8
	s_waitcnt lgkmcnt(0)
	v_max_f32_e32 v10, v10, v10
	v_max_f32_e32 v10, v7, v10
	ds_bpermute_b32 v35, v83, v10
	v_and_or_b32 v7, v2, s87, v6
	v_bfe_u32 v11, v15, 16, 1
	v_add3_u32 v34, v27, v34, s86
	v_and_or_b32 v5, v5, s87, v8
	s_waitcnt lgkmcnt(0)
	v_max_f32_e32 v2, v35, v35
	v_max_f32_e32 v2, v10, v2
	ds_bpermute_b32 v10, v84, v2
	v_add3_u32 v11, v15, v11, s86
	v_lshrrev_b32_e32 v34, 16, v34
	v_and_or_b32 v11, v11, s87, v34
	v_bfe_u32 v9, v16, 16, 1
	s_waitcnt lgkmcnt(0)
	v_max_f32_e32 v8, v10, v10
	v_max_f32_e32 v2, v2, v8
	ds_bpermute_b32 v34, v85, v2
	v_bfe_u32 v4, v22, 16, 1
	v_add3_u32 v9, v16, v9, s86
	v_add3_u32 v4, v22, v4, s86
	v_lshrrev_b32_e32 v9, 16, v9
	v_and_or_b32 v6, v4, s87, v9
	v_and_or_b32 v4, v53, s87, v62
	s_waitcnt lgkmcnt(0)
	v_max3_f32 v2, v2, v34, s55
	global_store_dwordx4 v[78:79], v[4:7], off
	v_bfe_u32 v31, v24, 16, 1
	v_bfe_u32 v32, v25, 16, 1
	v_div_scale_f32 v4, s[42:43], v2, v2, s80
	v_rcp_f32_e32 v5, v4
	v_bfe_u32 v33, v26, 16, 1
	v_bfe_u32 v18, v14, 16, 1
	v_bfe_u32 v19, v29, 16, 1
	v_bfe_u32 v30, v28, 16, 1
	v_add3_u32 v33, v26, v33, s86
	v_add3_u32 v32, v25, v32, s86
	v_add3_u32 v31, v24, v31, s86
	v_fma_f32 v7, -v4, v5, 1.0
	v_add3_u32 v30, v28, v30, s86
	v_add3_u32 v19, v29, v19, s86
	v_add3_u32 v18, v14, v18, s86
	v_lshrrev_b32_e32 v31, 16, v31
	v_lshrrev_b32_e32 v32, 16, v32
	v_lshrrev_b32_e32 v33, 16, v33
	v_div_scale_f32 v6, vcc, s80, v2, s80
	v_fmac_f32_e32 v5, v7, v5
	v_and_or_b32 v10, v18, s87, v33
	v_and_or_b32 v9, v19, s87, v32
	v_and_or_b32 v8, v30, s87, v31
	v_mul_f32_e32 v7, v6, v5
	global_store_dwordx4 v[78:79], v[8:11], off offset:1024
	s_nop 1
	v_fma_f32 v8, -v4, v7, v6
	v_fmac_f32_e32 v7, v8, v5
	v_fma_f32 v4, -v4, v7, v6
	v_div_fmas_f32 v4, v4, v5, v7
	v_div_fixup_f32 v4, v4, v2, s80
	v_mul_f32_e32 v5, v12, v4
	v_mul_f32_e32 v6, v20, v4
	v_rndne_f32_e32 v5, v5
	v_mul_f32_e32 v7, v13, v4
	v_mul_f32_e32 v8, v21, v4
	v_mul_f32_e32 v9, v16, v4
	v_mul_f32_e32 v10, v22, v4
	v_mul_f32_e32 v11, v17, v4
	v_mul_f32_e32 v12, v23, v4
	v_mul_f32_e32 v13, v24, v4
	v_mul_f32_e32 v16, v28, v4
	v_mul_f32_e32 v17, v25, v4
	v_mul_f32_e32 v18, v29, v4
	v_mul_f32_e32 v19, v26, v4
	v_mul_f32_e32 v14, v14, v4
	v_mul_f32_e32 v20, v27, v4
	v_mul_f32_e32 v4, v15, v4
	v_rndne_f32_e32 v6, v6
	v_rndne_f32_e32 v15, v4
	v_add_f32_e32 v4, 0x43000000, v5
	v_rndne_f32_e32 v7, v7
	v_cvt_pk_u8_f32 v4, v4, 0, 0
	v_add_f32_e32 v5, 0x43000000, v6
	v_rndne_f32_e32 v8, v8
	v_cvt_pk_u8_f32 v4, v5, 1, v4
	v_add_f32_e32 v5, 0x43000000, v7
	v_rndne_f32_e32 v9, v9
	v_cvt_pk_u8_f32 v4, v5, 2, v4
	v_add_f32_e32 v5, 0x43000000, v8
	v_rndne_f32_e32 v10, v10
	v_cvt_pk_u8_f32 v4, v5, 3, v4
	v_add_f32_e32 v5, 0x43000000, v9
	v_rndne_f32_e32 v11, v11
	v_cvt_pk_u8_f32 v5, v5, 0, 0
	v_add_f32_e32 v6, 0x43000000, v10
	v_rndne_f32_e32 v12, v12
	v_cvt_pk_u8_f32 v5, v6, 1, v5
	v_add_f32_e32 v6, 0x43000000, v11
	v_rndne_f32_e32 v13, v13
	v_cvt_pk_u8_f32 v5, v6, 2, v5
	v_add_f32_e32 v6, 0x43000000, v12
	v_rndne_f32_e32 v16, v16
	v_cvt_pk_u8_f32 v5, v6, 3, v5
	v_add_f32_e32 v6, 0x43000000, v13
	v_rndne_f32_e32 v17, v17
	v_cvt_pk_u8_f32 v6, v6, 0, 0
	v_add_f32_e32 v7, 0x43000000, v16
	v_rndne_f32_e32 v18, v18
	v_cvt_pk_u8_f32 v6, v7, 1, v6
	v_add_f32_e32 v7, 0x43000000, v17
	v_rndne_f32_e32 v19, v19
	v_cvt_pk_u8_f32 v6, v7, 2, v6
	v_add_f32_e32 v7, 0x43000000, v18
	v_rndne_f32_e32 v14, v14
	v_cvt_pk_u8_f32 v6, v7, 3, v6
	v_add_f32_e32 v7, 0x43000000, v19
	v_rndne_f32_e32 v20, v20
	v_cvt_pk_u8_f32 v7, v7, 0, 0
	v_add_f32_e32 v8, 0x43000000, v14
	v_cvt_pk_u8_f32 v7, v8, 1, v7
	v_add_f32_e32 v8, 0x43000000, v20
	v_cvt_pk_u8_f32 v7, v8, 2, v7
	v_add_f32_e32 v8, 0x43000000, v15
	v_xor_b32_e32 v4, 0x80808080, v4
	v_xor_b32_e32 v5, 0x80808080, v5
	v_cvt_pk_u8_f32 v7, v8, 3, v7
	v_lshl_add_u64 v[8:9], s[10:11], 0, v[38:39]
	v_xor_b32_e32 v6, 0x80808080, v6
	v_xor_b32_e32 v7, 0x80808080, v7
	global_store_dwordx2 v[8:9], v[4:5], off
	global_store_dwordx2 v[8:9], v[6:7], off offset:512
	s_and_saveexec_b64 s[10:11], s[4:5]
	s_cbranch_execz .LBB0_1206
	s_add_u32 s42, s18, s16
	s_addc_u32 s43, s19, s17
	v_mul_f32_e32 v2, 0x3c010204, v2
	global_store_dword v3, v2, s[42:43]
.LBB0_1206:
	s_or_b64 exec, exec, s[10:11]
	v_lshl_add_u64 v[78:79], s[18:19], 0, v[56:57]
	v_add_co_u32_e32 v4, vcc, 0x2f200000, v78
	s_mov_b32 s41, 0x2e00000
	s_nop 0
	v_addc_co_u32_e32 v5, vcc, 0, v79, vcc
	s_waitcnt vmcnt(5)
	v_mov_b64_e32 v[8:9], v[124:125]
	v_mov_b64_e32 v[10:11], v[126:127]
	v_mov_b64_e32 v[12:13], v[128:129]
	v_mov_b64_e32 v[14:15], v[130:131]
	v_lshl_add_u64 v[124:125], s[18:19], 0, v[54:55]
	v_add_co_u32_e32 v124, vcc, 0x2f200000, v124
	s_nop 1
	v_addc_co_u32_e32 v125, vcc, 0, v125, vcc
	global_load_dwordx4 v[128:131], v[124:125], off
	global_load_dwordx4 v[124:127], v[124:125], off offset:1024
	s_nop 0
	v_mov_b64_e32 v[4:5], v[160:161]
	v_mov_b64_e32 v[6:7], v[162:163]
	v_add_co_u32_e32 v78, vcc, s41, v78
	s_add_i32 s10, s40, 2
	s_nop 0
	v_addc_co_u32_e32 v79, vcc, 0, v79, vcc
	s_add_u32 s11, s30, s8
	s_addc_u32 s41, s31, s9
	s_add_i32 s42, s40, 0xffffc002
	s_cmpk_lt_i32 s10, 0x4000
	s_mov_b32 s10, 0x3e200000
	s_cselect_b32 s10, s10, 0x45200000
	s_cselect_b32 s43, s41, 0
	s_cselect_b32 s42, s11, s42
	s_add_u32 s41, s18, s10
	s_addc_u32 s44, s19, 0
	s_lshl_b64 s[10:11], s[42:43], 10
	s_add_u32 s10, s41, s10
	s_addc_u32 s11, s44, s11
	v_lshlrev_b32_e32 v62, 16, v8
	v_lshlrev_b32_e32 v70, 16, v12
	v_and_b32_e32 v72, 0xffff0000, v12
	v_add_f32_e32 v2, 0, v70
	v_lshlrev_b32_e32 v71, 16, v13
	v_add_f32_e32 v2, v2, v72
	v_and_b32_e32 v73, 0xffff0000, v13
	v_add_f32_e32 v2, v2, v71
	v_lshlrev_b32_e32 v74, 16, v14
	v_add_f32_e32 v2, v2, v73
	v_and_b32_e32 v76, 0xffff0000, v14
	v_add_f32_e32 v2, v2, v74
	v_lshlrev_b32_e32 v75, 16, v15
	v_add_f32_e32 v2, v2, v76
	v_and_b32_e32 v77, 0xffff0000, v15
	v_add_f32_e32 v2, v2, v75
	v_add_f32_e32 v2, v2, v77
	v_and_b32_e32 v64, 0xffff0000, v8
	v_add_f32_e32 v2, v2, v62
	v_lshlrev_b32_e32 v63, 16, v9
	v_add_f32_e32 v2, v2, v64
	v_and_b32_e32 v65, 0xffff0000, v9
	v_add_f32_e32 v2, v2, v63
	v_lshlrev_b32_e32 v66, 16, v10
	v_add_f32_e32 v2, v2, v65
	v_and_b32_e32 v68, 0xffff0000, v10
	v_add_f32_e32 v2, v2, v66
	v_lshlrev_b32_e32 v67, 16, v11
	v_add_f32_e32 v2, v2, v68
	v_and_b32_e32 v69, 0xffff0000, v11
	v_add_f32_e32 v2, v2, v67
	v_add_f32_e32 v2, v2, v69
	ds_bpermute_b32 v12, v80, v2
	v_mov_b64_e32 v[8:9], v[164:165]
	v_mov_b64_e32 v[10:11], v[166:167]
	s_waitcnt lgkmcnt(0)
	v_add_f32_e32 v2, v2, v12
	v_mov_b64_e32 v[12:13], v[168:169]
	v_mov_b64_e32 v[14:15], v[170:171]
	v_mov_b64_e32 v[16:17], v[172:173]
	v_mov_b64_e32 v[18:19], v[174:175]
	ds_bpermute_b32 v20, v81, v2
	s_waitcnt lgkmcnt(0)
	v_add_f32_e32 v2, v2, v20
	v_mov_b64_e32 v[20:21], v[176:177]
	v_mov_b64_e32 v[22:23], v[178:179]
	v_mov_b64_e32 v[24:25], v[180:181]
	v_mov_b64_e32 v[26:27], v[182:183]
	v_mov_b64_e32 v[28:29], v[184:185]
	v_mov_b64_e32 v[30:31], v[186:187]
	v_mov_b64_e32 v[32:33], v[188:189]
	v_mov_b64_e32 v[34:35], v[190:191]
	ds_bpermute_b32 v53, v82, v2
	s_waitcnt lgkmcnt(0)
	v_add_f32_e32 v2, v2, v53
	ds_bpermute_b32 v53, v83, v2
	s_waitcnt lgkmcnt(0)
	v_add_f32_e32 v2, v2, v53
	ds_bpermute_b32 v53, v84, v2
	s_waitcnt lgkmcnt(0)
	v_add_f32_e32 v2, v2, v53
	ds_bpermute_b32 v53, v85, v2
	s_waitcnt lgkmcnt(0)
	v_add_f32_e32 v2, v2, v53
	v_mul_f32_e32 v2, 0x3a800000, v2
	v_pk_add_f32 v[70:71], v[70:71], v[2:3] op_sel_hi:[1,0] neg_lo:[0,1] neg_hi:[0,1]
	v_pk_add_f32 v[72:73], v[72:73], v[2:3] op_sel_hi:[1,0] neg_lo:[0,1] neg_hi:[0,1]
	v_pk_mul_f32 v[108:109], v[70:71], v[70:71]
	v_pk_mul_f32 v[110:111], v[72:73], v[72:73]
	v_pk_add_f32 v[74:75], v[74:75], v[2:3] op_sel_hi:[1,0] neg_lo:[0,1] neg_hi:[0,1]
	v_pk_add_f32 v[76:77], v[76:77], v[2:3] op_sel_hi:[1,0] neg_lo:[0,1] neg_hi:[0,1]
	v_pk_add_f32 v[62:63], v[62:63], v[2:3] op_sel_hi:[1,0] neg_lo:[0,1] neg_hi:[0,1]
	v_pk_add_f32 v[64:65], v[64:65], v[2:3] op_sel_hi:[1,0] neg_lo:[0,1] neg_hi:[0,1]
	v_pk_add_f32 v[66:67], v[66:67], v[2:3] op_sel_hi:[1,0] neg_lo:[0,1] neg_hi:[0,1]
	v_pk_add_f32 v[68:69], v[68:69], v[2:3] op_sel_hi:[1,0] neg_lo:[0,1] neg_hi:[0,1]
	v_add_f32_e32 v2, v108, v110
	v_add_f32_e32 v2, v109, v2
	v_pk_mul_f32 v[112:113], v[74:75], v[74:75]
	v_add_f32_e32 v2, v111, v2
	v_pk_mul_f32 v[114:115], v[76:77], v[76:77]
	v_add_f32_e32 v2, v112, v2
	v_add_f32_e32 v2, v114, v2
	v_add_f32_e32 v2, v113, v2
	v_pk_mul_f32 v[116:117], v[62:63], v[62:63]
	v_add_f32_e32 v2, v115, v2
	v_pk_mul_f32 v[118:119], v[64:65], v[64:65]
	v_add_f32_e32 v2, v116, v2
	v_add_f32_e32 v2, v118, v2
	v_mov_b32_e32 v120, v68
	v_mov_b32_e32 v121, v66
	v_add_f32_e32 v2, v117, v2
	v_pk_mul_f32 v[120:121], v[120:121], v[120:121]
	v_add_f32_e32 v2, v119, v2
	v_mov_b32_e32 v122, v69
	v_mov_b32_e32 v123, v67
	v_add_f32_e32 v2, v121, v2
	v_pk_mul_f32 v[122:123], v[122:123], v[122:123]
	v_add_f32_e32 v2, v120, v2
	v_add_f32_e32 v2, v123, v2
	v_add_f32_e32 v2, v122, v2
	ds_bpermute_b32 v53, v80, v2
	v_mov_b32_e32 v108, v4
	v_mov_b32_e32 v109, v6
	v_mov_b32_e32 v6, v5
	s_waitcnt lgkmcnt(0)
	v_add_f32_e32 v2, v2, v53
	ds_bpermute_b32 v4, v81, v2
	v_mov_b32_e32 v110, v8
	v_mov_b32_e32 v111, v10
	v_mov_b32_e32 v10, v9
	s_waitcnt lgkmcnt(0)
	v_add_f32_e32 v2, v2, v4
	ds_bpermute_b32 v53, v82, v2
	v_mov_b32_e32 v8, v16
	v_mov_b32_e32 v4, v12
	v_mov_b32_e32 v5, v14
	v_mov_b32_e32 v9, v18
	s_waitcnt lgkmcnt(0)
	v_add_f32_e32 v2, v2, v53
	ds_bpermute_b32 v16, v83, v2
	v_mov_b32_e32 v12, v24
	v_mov_b32_e32 v14, v13
	v_mov_b32_e32 v18, v17
	v_mov_b32_e32 v13, v26
	s_waitcnt lgkmcnt(0)
	v_add_f32_e32 v2, v2, v16
	ds_bpermute_b32 v24, v84, v2
	v_mov_b32_e32 v16, v32
	v_mov_b32_e32 v17, v34
	v_mov_b32_e32 v26, v25
	v_mov_b32_e32 v34, v33
	s_waitcnt lgkmcnt(0)
	v_add_f32_e32 v2, v2, v24
	ds_bpermute_b32 v53, v85, v2
	v_mov_b32_e32 v24, v20
	v_mov_b32_e32 v25, v22
	v_mov_b32_e32 v32, v28
	v_mov_b32_e32 v33, v30
	s_waitcnt lgkmcnt(0)
	v_add_f32_e32 v2, v2, v53
	v_fmamk_f32 v2, v2, 0x3a800000, v237
	v_mul_f32_e32 v20, 0x4b800000, v2
	v_cmp_gt_f32_e32 vcc, s85, v2
	v_mov_b32_e32 v22, v21
	v_mov_b32_e32 v30, v29
	v_cndmask_b32_e32 v2, v2, v20, vcc
	v_rsq_f32_e32 v2, v2
	s_nop 0
	v_mul_f32_e32 v20, 0x45800000, v2
	v_cndmask_b32_e32 v2, v2, v20, vcc
	v_pk_mul_f32 v[20:21], v[70:71], v[2:3] op_sel_hi:[1,0]
	v_pk_mul_f32 v[28:29], v[74:75], v[2:3] op_sel_hi:[1,0]
	v_pk_mul_f32 v[70:71], v[72:73], v[2:3] op_sel_hi:[1,0]
	v_pk_mul_f32 v[64:65], v[64:65], v[2:3] op_sel_hi:[1,0]
	v_pk_fma_f32 v[12:13], v[12:13], v[20:21], v[16:17]
	v_pk_fma_f32 v[16:17], v[24:25], v[28:29], v[32:33]
	v_pk_fma_f32 v[20:21], v[26:27], v[70:71], v[34:35]
	v_pk_mul_f32 v[72:73], v[76:77], v[2:3] op_sel_hi:[1,0]
	v_pk_fma_f32 v[28:29], v[6:7], v[64:65], v[10:11]
	v_bfe_u32 v6, v20, 16, 1
	v_bfe_u32 v10, v17, 16, 1
	v_max3_f32 v35, |v12|, 0, |v20|
	v_pk_fma_f32 v[22:23], v[22:23], v[72:73], v[30:31]
	v_add3_u32 v53, v20, v6, s86
	v_add3_u32 v6, v17, v10, s86
	v_max3_f32 v10, v35, |v13|, |v21|
	v_pk_mul_f32 v[62:63], v[62:63], v[2:3] op_sel_hi:[1,0]
	v_max3_f32 v10, v10, |v16|, |v22|
	v_pk_fma_f32 v[24:25], v[108:109], v[62:63], v[110:111]
	v_max3_f32 v10, v10, |v17|, |v23|
	v_pk_mul_f32 v[66:67], v[66:67], v[2:3] op_sel_hi:[1,0]
	v_pk_mul_f32 v[68:69], v[68:69], v[2:3] op_sel_hi:[1,0]
	v_max3_f32 v10, v10, |v24|, |v28|
	v_pk_fma_f32 v[26:27], v[4:5], v[66:67], v[8:9]
	v_pk_fma_f32 v[14:15], v[14:15], v[68:69], v[18:19]
	v_max3_f32 v10, v10, |v25|, |v29|
	v_max3_f32 v10, v10, |v26|, |v14|
	v_max3_f32 v10, v10, |v27|, |v15|
	ds_bpermute_b32 v35, v80, v10
	v_bfe_u32 v7, v12, 16, 1
	v_add3_u32 v7, v12, v7, s86
	v_lshrrev_b32_e32 v62, 16, v7
	v_bfe_u32 v2, v23, 16, 1
	s_waitcnt lgkmcnt(0)
	v_max_f32_e32 v35, v35, v35
	v_max_f32_e32 v10, v10, v35
	ds_bpermute_b32 v35, v81, v10
	v_add3_u32 v2, v23, v2, s86
	v_lshrrev_b32_e32 v6, 16, v6
	v_bfe_u32 v8, v13, 16, 1
	v_bfe_u32 v5, v21, 16, 1
	s_waitcnt lgkmcnt(0)
	v_max_f32_e32 v7, v35, v35
	v_max_f32_e32 v7, v10, v7
	ds_bpermute_b32 v10, v82, v7
	v_add3_u32 v8, v13, v8, s86
	v_bfe_u32 v34, v27, 16, 1
	v_add3_u32 v5, v21, v5, s86
	v_lshrrev_b32_e32 v8, 16, v8
	s_waitcnt lgkmcnt(0)
	v_max_f32_e32 v10, v10, v10
	v_max_f32_e32 v10, v7, v10
	ds_bpermute_b32 v35, v83, v10
	v_and_or_b32 v7, v2, s87, v6
	v_bfe_u32 v11, v15, 16, 1
	v_add3_u32 v34, v27, v34, s86
	v_and_or_b32 v5, v5, s87, v8
	s_waitcnt lgkmcnt(0)
	v_max_f32_e32 v2, v35, v35
	v_max_f32_e32 v2, v10, v2
	ds_bpermute_b32 v10, v84, v2
	v_add3_u32 v11, v15, v11, s86
	v_lshrrev_b32_e32 v34, 16, v34
	v_and_or_b32 v11, v11, s87, v34
	v_bfe_u32 v9, v16, 16, 1
	s_waitcnt lgkmcnt(0)
	v_max_f32_e32 v8, v10, v10
	v_max_f32_e32 v2, v2, v8
	ds_bpermute_b32 v34, v85, v2
	v_bfe_u32 v4, v22, 16, 1
	v_add3_u32 v9, v16, v9, s86
	v_add3_u32 v4, v22, v4, s86
	v_lshrrev_b32_e32 v9, 16, v9
	v_and_or_b32 v6, v4, s87, v9
	v_and_or_b32 v4, v53, s87, v62
	s_waitcnt lgkmcnt(0)
	v_max3_f32 v2, v2, v34, s55
	global_store_dwordx4 v[78:79], v[4:7], off
	v_bfe_u32 v31, v24, 16, 1
	v_bfe_u32 v32, v25, 16, 1
	v_div_scale_f32 v4, s[42:43], v2, v2, s80
	v_rcp_f32_e32 v5, v4
	v_bfe_u32 v33, v26, 16, 1
	v_bfe_u32 v18, v14, 16, 1
	v_bfe_u32 v19, v29, 16, 1
	v_bfe_u32 v30, v28, 16, 1
	v_add3_u32 v33, v26, v33, s86
	v_add3_u32 v32, v25, v32, s86
	v_add3_u32 v31, v24, v31, s86
	v_fma_f32 v7, -v4, v5, 1.0
	v_add3_u32 v30, v28, v30, s86
	v_add3_u32 v19, v29, v19, s86
	v_add3_u32 v18, v14, v18, s86
	v_lshrrev_b32_e32 v31, 16, v31
	v_lshrrev_b32_e32 v32, 16, v32
	v_lshrrev_b32_e32 v33, 16, v33
	v_div_scale_f32 v6, vcc, s80, v2, s80
	v_fmac_f32_e32 v5, v7, v5
	v_and_or_b32 v10, v18, s87, v33
	v_and_or_b32 v9, v19, s87, v32
	v_and_or_b32 v8, v30, s87, v31
	v_mul_f32_e32 v7, v6, v5
	global_store_dwordx4 v[78:79], v[8:11], off offset:1024
	s_nop 1
	v_fma_f32 v8, -v4, v7, v6
	v_fmac_f32_e32 v7, v8, v5
	v_fma_f32 v4, -v4, v7, v6
	v_div_fmas_f32 v4, v4, v5, v7
	v_div_fixup_f32 v4, v4, v2, s80
	v_mul_f32_e32 v5, v12, v4
	v_mul_f32_e32 v6, v20, v4
	v_rndne_f32_e32 v5, v5
	v_mul_f32_e32 v7, v13, v4
	v_mul_f32_e32 v8, v21, v4
	v_mul_f32_e32 v9, v16, v4
	v_mul_f32_e32 v10, v22, v4
	v_mul_f32_e32 v11, v17, v4
	v_mul_f32_e32 v12, v23, v4
	v_mul_f32_e32 v13, v24, v4
	v_mul_f32_e32 v16, v28, v4
	v_mul_f32_e32 v17, v25, v4
	v_mul_f32_e32 v18, v29, v4
	v_mul_f32_e32 v19, v26, v4
	v_mul_f32_e32 v14, v14, v4
	v_mul_f32_e32 v20, v27, v4
	v_mul_f32_e32 v4, v15, v4
	v_rndne_f32_e32 v6, v6
	v_rndne_f32_e32 v15, v4
	v_add_f32_e32 v4, 0x43000000, v5
	v_rndne_f32_e32 v7, v7
	v_cvt_pk_u8_f32 v4, v4, 0, 0
	v_add_f32_e32 v5, 0x43000000, v6
	v_rndne_f32_e32 v8, v8
	v_cvt_pk_u8_f32 v4, v5, 1, v4
	v_add_f32_e32 v5, 0x43000000, v7
	v_rndne_f32_e32 v9, v9
	v_cvt_pk_u8_f32 v4, v5, 2, v4
	v_add_f32_e32 v5, 0x43000000, v8
	v_rndne_f32_e32 v10, v10
	v_cvt_pk_u8_f32 v4, v5, 3, v4
	v_add_f32_e32 v5, 0x43000000, v9
	v_rndne_f32_e32 v11, v11
	v_cvt_pk_u8_f32 v5, v5, 0, 0
	v_add_f32_e32 v6, 0x43000000, v10
	v_rndne_f32_e32 v12, v12
	v_cvt_pk_u8_f32 v5, v6, 1, v5
	v_add_f32_e32 v6, 0x43000000, v11
	v_rndne_f32_e32 v13, v13
	v_cvt_pk_u8_f32 v5, v6, 2, v5
	v_add_f32_e32 v6, 0x43000000, v12
	v_rndne_f32_e32 v16, v16
	v_cvt_pk_u8_f32 v5, v6, 3, v5
	v_add_f32_e32 v6, 0x43000000, v13
	v_rndne_f32_e32 v17, v17
	v_cvt_pk_u8_f32 v6, v6, 0, 0
	v_add_f32_e32 v7, 0x43000000, v16
	v_rndne_f32_e32 v18, v18
	v_cvt_pk_u8_f32 v6, v7, 1, v6
	v_add_f32_e32 v7, 0x43000000, v17
	v_rndne_f32_e32 v19, v19
	v_cvt_pk_u8_f32 v6, v7, 2, v6
	v_add_f32_e32 v7, 0x43000000, v18
	v_rndne_f32_e32 v14, v14
	v_cvt_pk_u8_f32 v6, v7, 3, v6
	v_add_f32_e32 v7, 0x43000000, v19
	v_rndne_f32_e32 v20, v20
	v_cvt_pk_u8_f32 v7, v7, 0, 0
	v_add_f32_e32 v8, 0x43000000, v14
	v_cvt_pk_u8_f32 v7, v8, 1, v7
	v_add_f32_e32 v8, 0x43000000, v20
	v_cvt_pk_u8_f32 v7, v8, 2, v7
	v_add_f32_e32 v8, 0x43000000, v15
	v_xor_b32_e32 v4, 0x80808080, v4
	v_xor_b32_e32 v5, 0x80808080, v5
	v_cvt_pk_u8_f32 v7, v8, 3, v7
	v_lshl_add_u64 v[8:9], s[10:11], 0, v[38:39]
	v_xor_b32_e32 v6, 0x80808080, v6
	v_xor_b32_e32 v7, 0x80808080, v7
	global_store_dwordx2 v[8:9], v[4:5], off
	global_store_dwordx2 v[8:9], v[6:7], off offset:512
	s_and_saveexec_b64 s[10:11], s[4:5]
	s_cbranch_execz .LBB0_1208
	s_add_u32 s42, s18, s14
	s_addc_u32 s43, s19, s15
	v_mul_f32_e32 v2, 0x3c010204, v2
	global_store_dword v3, v2, s[42:43]
.LBB0_1208:
	s_or_b64 exec, exec, s[10:11]
	v_lshl_add_u64 v[78:79], s[18:19], 0, v[54:55]
	v_add_co_u32_e32 v4, vcc, 0x2f200000, v78
	s_mov_b32 s41, 0x2e00000
	s_nop 0
	v_addc_co_u32_e32 v5, vcc, 0, v79, vcc
	s_waitcnt vmcnt(5)
	v_mov_b64_e32 v[8:9], v[124:125]
	v_mov_b64_e32 v[10:11], v[126:127]
	v_mov_b64_e32 v[12:13], v[128:129]
	v_mov_b64_e32 v[14:15], v[130:131]
	v_lshl_add_u64 v[124:125], s[18:19], 0, v[60:61]
	v_add_co_u32_e32 v124, vcc, 0x2f202000, v124
	s_nop 1
	v_addc_co_u32_e32 v125, vcc, 0, v125, vcc
	global_load_dwordx4 v[128:131], v[124:125], off
	global_load_dwordx4 v[124:127], v[124:125], off offset:1024
	s_nop 0
	v_mov_b64_e32 v[4:5], v[160:161]
	v_mov_b64_e32 v[6:7], v[162:163]
	v_add_co_u32_e32 v78, vcc, s41, v78
	s_add_i32 s10, s40, 3
	s_nop 0
	v_addc_co_u32_e32 v79, vcc, 0, v79, vcc
	s_add_u32 s11, s28, s8
	s_addc_u32 s41, s29, s9
	s_addk_i32 s40, 0xc003
	s_cmpk_lt_i32 s10, 0x4000
	s_mov_b32 s10, 0x3e200000
	s_cselect_b32 s10, s10, 0x45200000
	s_cselect_b32 s41, s41, 0
	s_cselect_b32 s40, s11, s40
	s_add_u32 s42, s18, s10
	s_addc_u32 s43, s19, 0
	s_lshl_b64 s[10:11], s[40:41], 10
	s_add_u32 s10, s42, s10
	s_addc_u32 s11, s43, s11
	v_lshlrev_b32_e32 v62, 16, v8
	v_lshlrev_b32_e32 v70, 16, v12
	v_and_b32_e32 v72, 0xffff0000, v12
	v_add_f32_e32 v2, 0, v70
	v_lshlrev_b32_e32 v71, 16, v13
	v_add_f32_e32 v2, v2, v72
	v_and_b32_e32 v73, 0xffff0000, v13
	v_add_f32_e32 v2, v2, v71
	v_lshlrev_b32_e32 v74, 16, v14
	v_add_f32_e32 v2, v2, v73
	v_and_b32_e32 v76, 0xffff0000, v14
	v_add_f32_e32 v2, v2, v74
	v_lshlrev_b32_e32 v75, 16, v15
	v_add_f32_e32 v2, v2, v76
	v_and_b32_e32 v77, 0xffff0000, v15
	v_add_f32_e32 v2, v2, v75
	v_add_f32_e32 v2, v2, v77
	v_and_b32_e32 v64, 0xffff0000, v8
	v_add_f32_e32 v2, v2, v62
	v_lshlrev_b32_e32 v63, 16, v9
	v_add_f32_e32 v2, v2, v64
	v_and_b32_e32 v65, 0xffff0000, v9
	v_add_f32_e32 v2, v2, v63
	v_lshlrev_b32_e32 v66, 16, v10
	v_add_f32_e32 v2, v2, v65
	v_and_b32_e32 v68, 0xffff0000, v10
	v_add_f32_e32 v2, v2, v66
	v_lshlrev_b32_e32 v67, 16, v11
	v_add_f32_e32 v2, v2, v68
	v_and_b32_e32 v69, 0xffff0000, v11
	v_add_f32_e32 v2, v2, v67
	v_add_f32_e32 v2, v2, v69
	ds_bpermute_b32 v12, v80, v2
	v_mov_b64_e32 v[8:9], v[164:165]
	v_mov_b64_e32 v[10:11], v[166:167]
	s_waitcnt lgkmcnt(0)
	v_add_f32_e32 v2, v2, v12
	v_mov_b64_e32 v[12:13], v[168:169]
	v_mov_b64_e32 v[14:15], v[170:171]
	v_mov_b64_e32 v[16:17], v[172:173]
	v_mov_b64_e32 v[18:19], v[174:175]
	ds_bpermute_b32 v20, v81, v2
	s_waitcnt lgkmcnt(0)
	v_add_f32_e32 v2, v2, v20
	v_mov_b64_e32 v[20:21], v[176:177]
	v_mov_b64_e32 v[22:23], v[178:179]
	v_mov_b64_e32 v[24:25], v[180:181]
	v_mov_b64_e32 v[26:27], v[182:183]
	v_mov_b64_e32 v[28:29], v[184:185]
	v_mov_b64_e32 v[30:31], v[186:187]
	v_mov_b64_e32 v[32:33], v[188:189]
	v_mov_b64_e32 v[34:35], v[190:191]
	ds_bpermute_b32 v53, v82, v2
	s_waitcnt lgkmcnt(0)
	v_add_f32_e32 v2, v2, v53
	ds_bpermute_b32 v53, v83, v2
	s_waitcnt lgkmcnt(0)
	v_add_f32_e32 v2, v2, v53
	ds_bpermute_b32 v53, v84, v2
	s_waitcnt lgkmcnt(0)
	v_add_f32_e32 v2, v2, v53
	ds_bpermute_b32 v53, v85, v2
	s_waitcnt lgkmcnt(0)
	v_add_f32_e32 v2, v2, v53
	v_mul_f32_e32 v2, 0x3a800000, v2
	v_pk_add_f32 v[70:71], v[70:71], v[2:3] op_sel_hi:[1,0] neg_lo:[0,1] neg_hi:[0,1]
	v_pk_add_f32 v[72:73], v[72:73], v[2:3] op_sel_hi:[1,0] neg_lo:[0,1] neg_hi:[0,1]
	v_pk_mul_f32 v[108:109], v[70:71], v[70:71]
	v_pk_mul_f32 v[110:111], v[72:73], v[72:73]
	v_pk_add_f32 v[74:75], v[74:75], v[2:3] op_sel_hi:[1,0] neg_lo:[0,1] neg_hi:[0,1]
	v_pk_add_f32 v[76:77], v[76:77], v[2:3] op_sel_hi:[1,0] neg_lo:[0,1] neg_hi:[0,1]
	v_pk_add_f32 v[62:63], v[62:63], v[2:3] op_sel_hi:[1,0] neg_lo:[0,1] neg_hi:[0,1]
	v_pk_add_f32 v[64:65], v[64:65], v[2:3] op_sel_hi:[1,0] neg_lo:[0,1] neg_hi:[0,1]
	v_pk_add_f32 v[66:67], v[66:67], v[2:3] op_sel_hi:[1,0] neg_lo:[0,1] neg_hi:[0,1]
	v_pk_add_f32 v[68:69], v[68:69], v[2:3] op_sel_hi:[1,0] neg_lo:[0,1] neg_hi:[0,1]
	v_add_f32_e32 v2, v108, v110
	v_add_f32_e32 v2, v109, v2
	v_pk_mul_f32 v[112:113], v[74:75], v[74:75]
	v_add_f32_e32 v2, v111, v2
	v_pk_mul_f32 v[114:115], v[76:77], v[76:77]
	v_add_f32_e32 v2, v112, v2
	v_add_f32_e32 v2, v114, v2
	v_add_f32_e32 v2, v113, v2
	v_pk_mul_f32 v[116:117], v[62:63], v[62:63]
	v_add_f32_e32 v2, v115, v2
	v_pk_mul_f32 v[118:119], v[64:65], v[64:65]
	v_add_f32_e32 v2, v116, v2
	v_add_f32_e32 v2, v118, v2
	v_mov_b32_e32 v120, v68
	v_mov_b32_e32 v121, v66
	v_add_f32_e32 v2, v117, v2
	v_pk_mul_f32 v[120:121], v[120:121], v[120:121]
	v_add_f32_e32 v2, v119, v2
	v_mov_b32_e32 v122, v69
	v_mov_b32_e32 v123, v67
	v_add_f32_e32 v2, v121, v2
	v_pk_mul_f32 v[122:123], v[122:123], v[122:123]
	v_add_f32_e32 v2, v120, v2
	v_add_f32_e32 v2, v123, v2
	v_add_f32_e32 v2, v122, v2
	ds_bpermute_b32 v53, v80, v2
	v_mov_b32_e32 v108, v4
	v_mov_b32_e32 v109, v6
	v_mov_b32_e32 v6, v5
	s_waitcnt lgkmcnt(0)
	v_add_f32_e32 v2, v2, v53
	ds_bpermute_b32 v4, v81, v2
	v_mov_b32_e32 v110, v8
	v_mov_b32_e32 v111, v10
	v_mov_b32_e32 v10, v9
	s_waitcnt lgkmcnt(0)
	v_add_f32_e32 v2, v2, v4
	ds_bpermute_b32 v53, v82, v2
	v_mov_b32_e32 v8, v16
	v_mov_b32_e32 v4, v12
	v_mov_b32_e32 v5, v14
	v_mov_b32_e32 v9, v18
	s_waitcnt lgkmcnt(0)
	v_add_f32_e32 v2, v2, v53
	ds_bpermute_b32 v16, v83, v2
	v_mov_b32_e32 v12, v24
	v_mov_b32_e32 v14, v13
	v_mov_b32_e32 v18, v17
	v_mov_b32_e32 v13, v26
	s_waitcnt lgkmcnt(0)
	v_add_f32_e32 v2, v2, v16
	ds_bpermute_b32 v24, v84, v2
	v_mov_b32_e32 v16, v32
	v_mov_b32_e32 v17, v34
	v_mov_b32_e32 v26, v25
	v_mov_b32_e32 v34, v33
	s_waitcnt lgkmcnt(0)
	v_add_f32_e32 v2, v2, v24
	ds_bpermute_b32 v53, v85, v2
	v_mov_b32_e32 v24, v20
	v_mov_b32_e32 v25, v22
	v_mov_b32_e32 v32, v28
	v_mov_b32_e32 v33, v30
	s_waitcnt lgkmcnt(0)
	v_add_f32_e32 v2, v2, v53
	v_fmamk_f32 v2, v2, 0x3a800000, v237
	v_mul_f32_e32 v20, 0x4b800000, v2
	v_cmp_gt_f32_e32 vcc, s85, v2
	v_mov_b32_e32 v22, v21
	v_mov_b32_e32 v30, v29
	v_cndmask_b32_e32 v2, v2, v20, vcc
	v_rsq_f32_e32 v2, v2
	s_nop 0
	v_mul_f32_e32 v20, 0x45800000, v2
	v_cndmask_b32_e32 v2, v2, v20, vcc
	v_pk_mul_f32 v[20:21], v[70:71], v[2:3] op_sel_hi:[1,0]
	v_pk_mul_f32 v[28:29], v[74:75], v[2:3] op_sel_hi:[1,0]
	v_pk_mul_f32 v[70:71], v[72:73], v[2:3] op_sel_hi:[1,0]
	v_pk_mul_f32 v[64:65], v[64:65], v[2:3] op_sel_hi:[1,0]
	v_pk_fma_f32 v[12:13], v[12:13], v[20:21], v[16:17]
	v_pk_fma_f32 v[16:17], v[24:25], v[28:29], v[32:33]
	v_pk_fma_f32 v[20:21], v[26:27], v[70:71], v[34:35]
	v_pk_mul_f32 v[72:73], v[76:77], v[2:3] op_sel_hi:[1,0]
	v_pk_fma_f32 v[28:29], v[6:7], v[64:65], v[10:11]
	v_bfe_u32 v6, v20, 16, 1
	v_bfe_u32 v10, v17, 16, 1
	v_max3_f32 v35, |v12|, 0, |v20|
	v_pk_fma_f32 v[22:23], v[22:23], v[72:73], v[30:31]
	v_add3_u32 v53, v20, v6, s86
	v_add3_u32 v6, v17, v10, s86
	v_max3_f32 v10, v35, |v13|, |v21|
	v_pk_mul_f32 v[62:63], v[62:63], v[2:3] op_sel_hi:[1,0]
	v_max3_f32 v10, v10, |v16|, |v22|
	v_pk_fma_f32 v[24:25], v[108:109], v[62:63], v[110:111]
	v_max3_f32 v10, v10, |v17|, |v23|
	v_pk_mul_f32 v[66:67], v[66:67], v[2:3] op_sel_hi:[1,0]
	v_pk_mul_f32 v[68:69], v[68:69], v[2:3] op_sel_hi:[1,0]
	v_max3_f32 v10, v10, |v24|, |v28|
	v_pk_fma_f32 v[26:27], v[4:5], v[66:67], v[8:9]
	v_pk_fma_f32 v[14:15], v[14:15], v[68:69], v[18:19]
	v_max3_f32 v10, v10, |v25|, |v29|
	v_max3_f32 v10, v10, |v26|, |v14|
	v_max3_f32 v10, v10, |v27|, |v15|
	ds_bpermute_b32 v35, v80, v10
	v_bfe_u32 v7, v12, 16, 1
	v_add3_u32 v7, v12, v7, s86
	v_lshrrev_b32_e32 v62, 16, v7
	v_bfe_u32 v2, v23, 16, 1
	s_waitcnt lgkmcnt(0)
	v_max_f32_e32 v35, v35, v35
	v_max_f32_e32 v10, v10, v35
	ds_bpermute_b32 v35, v81, v10
	v_add3_u32 v2, v23, v2, s86
	v_lshrrev_b32_e32 v6, 16, v6
	v_bfe_u32 v8, v13, 16, 1
	v_bfe_u32 v5, v21, 16, 1
	s_waitcnt lgkmcnt(0)
	v_max_f32_e32 v7, v35, v35
	v_max_f32_e32 v7, v10, v7
	ds_bpermute_b32 v10, v82, v7
	v_add3_u32 v8, v13, v8, s86
	v_bfe_u32 v34, v27, 16, 1
	v_add3_u32 v5, v21, v5, s86
	v_lshrrev_b32_e32 v8, 16, v8
	s_waitcnt lgkmcnt(0)
	v_max_f32_e32 v10, v10, v10
	v_max_f32_e32 v10, v7, v10
	ds_bpermute_b32 v35, v83, v10
	v_and_or_b32 v7, v2, s87, v6
	v_bfe_u32 v11, v15, 16, 1
	v_add3_u32 v34, v27, v34, s86
	v_and_or_b32 v5, v5, s87, v8
	s_waitcnt lgkmcnt(0)
	v_max_f32_e32 v2, v35, v35
	v_max_f32_e32 v2, v10, v2
	ds_bpermute_b32 v10, v84, v2
	v_add3_u32 v11, v15, v11, s86
	v_lshrrev_b32_e32 v34, 16, v34
	v_and_or_b32 v11, v11, s87, v34
	v_bfe_u32 v9, v16, 16, 1
	s_waitcnt lgkmcnt(0)
	v_max_f32_e32 v8, v10, v10
	v_max_f32_e32 v2, v2, v8
	ds_bpermute_b32 v34, v85, v2
	v_bfe_u32 v4, v22, 16, 1
	v_add3_u32 v9, v16, v9, s86
	v_add3_u32 v4, v22, v4, s86
	v_lshrrev_b32_e32 v9, 16, v9
	v_and_or_b32 v6, v4, s87, v9
	v_and_or_b32 v4, v53, s87, v62
	s_waitcnt lgkmcnt(0)
	v_max3_f32 v2, v2, v34, s55
	global_store_dwordx4 v[78:79], v[4:7], off
	v_bfe_u32 v31, v24, 16, 1
	v_bfe_u32 v32, v25, 16, 1
	v_div_scale_f32 v4, s[40:41], v2, v2, s80
	v_rcp_f32_e32 v5, v4
	v_bfe_u32 v33, v26, 16, 1
	v_bfe_u32 v18, v14, 16, 1
	v_bfe_u32 v19, v29, 16, 1
	v_bfe_u32 v30, v28, 16, 1
	v_add3_u32 v33, v26, v33, s86
	v_add3_u32 v32, v25, v32, s86
	v_add3_u32 v31, v24, v31, s86
	v_fma_f32 v7, -v4, v5, 1.0
	v_add3_u32 v30, v28, v30, s86
	v_add3_u32 v19, v29, v19, s86
	v_add3_u32 v18, v14, v18, s86
	v_lshrrev_b32_e32 v31, 16, v31
	v_lshrrev_b32_e32 v32, 16, v32
	v_lshrrev_b32_e32 v33, 16, v33
	v_div_scale_f32 v6, vcc, s80, v2, s80
	v_fmac_f32_e32 v5, v7, v5
	v_and_or_b32 v10, v18, s87, v33
	v_and_or_b32 v9, v19, s87, v32
	v_and_or_b32 v8, v30, s87, v31
	v_mul_f32_e32 v7, v6, v5
	global_store_dwordx4 v[78:79], v[8:11], off offset:1024
	s_nop 1
	v_fma_f32 v8, -v4, v7, v6
	v_fmac_f32_e32 v7, v8, v5
	v_fma_f32 v4, -v4, v7, v6
	v_div_fmas_f32 v4, v4, v5, v7
	v_div_fixup_f32 v4, v4, v2, s80
	v_mul_f32_e32 v5, v12, v4
	v_mul_f32_e32 v6, v20, v4
	v_rndne_f32_e32 v5, v5
	v_mul_f32_e32 v7, v13, v4
	v_mul_f32_e32 v8, v21, v4
	v_mul_f32_e32 v9, v16, v4
	v_mul_f32_e32 v10, v22, v4
	v_mul_f32_e32 v11, v17, v4
	v_mul_f32_e32 v12, v23, v4
	v_mul_f32_e32 v13, v24, v4
	v_mul_f32_e32 v16, v28, v4
	v_mul_f32_e32 v17, v25, v4
	v_mul_f32_e32 v18, v29, v4
	v_mul_f32_e32 v19, v26, v4
	v_mul_f32_e32 v14, v14, v4
	v_mul_f32_e32 v20, v27, v4
	v_mul_f32_e32 v4, v15, v4
	v_rndne_f32_e32 v6, v6
	v_rndne_f32_e32 v15, v4
	v_add_f32_e32 v4, 0x43000000, v5
	v_rndne_f32_e32 v7, v7
	v_cvt_pk_u8_f32 v4, v4, 0, 0
	v_add_f32_e32 v5, 0x43000000, v6
	v_rndne_f32_e32 v8, v8
	v_cvt_pk_u8_f32 v4, v5, 1, v4
	v_add_f32_e32 v5, 0x43000000, v7
	v_rndne_f32_e32 v9, v9
	v_cvt_pk_u8_f32 v4, v5, 2, v4
	v_add_f32_e32 v5, 0x43000000, v8
	v_rndne_f32_e32 v10, v10
	v_cvt_pk_u8_f32 v4, v5, 3, v4
	v_add_f32_e32 v5, 0x43000000, v9
	v_rndne_f32_e32 v11, v11
	v_cvt_pk_u8_f32 v5, v5, 0, 0
	v_add_f32_e32 v6, 0x43000000, v10
	v_rndne_f32_e32 v12, v12
	v_cvt_pk_u8_f32 v5, v6, 1, v5
	v_add_f32_e32 v6, 0x43000000, v11
	v_rndne_f32_e32 v13, v13
	v_cvt_pk_u8_f32 v5, v6, 2, v5
	v_add_f32_e32 v6, 0x43000000, v12
	v_rndne_f32_e32 v16, v16
	v_cvt_pk_u8_f32 v5, v6, 3, v5
	v_add_f32_e32 v6, 0x43000000, v13
	v_rndne_f32_e32 v17, v17
	v_cvt_pk_u8_f32 v6, v6, 0, 0
	v_add_f32_e32 v7, 0x43000000, v16
	v_rndne_f32_e32 v18, v18
	v_cvt_pk_u8_f32 v6, v7, 1, v6
	v_add_f32_e32 v7, 0x43000000, v17
	v_rndne_f32_e32 v19, v19
	v_cvt_pk_u8_f32 v6, v7, 2, v6
	v_add_f32_e32 v7, 0x43000000, v18
	v_rndne_f32_e32 v14, v14
	v_cvt_pk_u8_f32 v6, v7, 3, v6
	v_add_f32_e32 v7, 0x43000000, v19
	v_rndne_f32_e32 v20, v20
	v_cvt_pk_u8_f32 v7, v7, 0, 0
	v_add_f32_e32 v8, 0x43000000, v14
	v_cvt_pk_u8_f32 v7, v8, 1, v7
	v_add_f32_e32 v8, 0x43000000, v20
	v_cvt_pk_u8_f32 v7, v8, 2, v7
	v_add_f32_e32 v8, 0x43000000, v15
	v_xor_b32_e32 v4, 0x80808080, v4
	v_xor_b32_e32 v5, 0x80808080, v5
	v_cvt_pk_u8_f32 v7, v8, 3, v7
	v_lshl_add_u64 v[8:9], s[10:11], 0, v[38:39]
	v_xor_b32_e32 v6, 0x80808080, v6
	v_xor_b32_e32 v7, 0x80808080, v7
	global_store_dwordx2 v[8:9], v[4:5], off
	global_store_dwordx2 v[8:9], v[6:7], off offset:512
	s_and_saveexec_b64 s[10:11], s[4:5]
	s_cbranch_execz .LBB0_1201
	s_add_u32 s40, s18, s12
	s_addc_u32 s41, s19, s13
	v_mul_f32_e32 v2, 0x3c010204, v2
	global_store_dword v3, v2, s[40:41]
	s_branch .LBB0_1201
